# baseline (speedup 1.0000x reference)
_Z16sum_layer_kernelPKfS0_Pf:
	s_load_dwordx4 s[4:7], s[0:1], 0x0
	s_load_dwordx2 s[8:9], s[0:1], 0x10
	v_and_b32_e32 v40, 31, v0
	v_bfe_u32 v41, v0, 5, 1
	v_lshrrev_b32_e32 v42, 6, v0
	v_and_b32_e32 v43, 7, v0
	v_bfe_u32 v44, v0, 3, 3
	v_and_b32_e32 v45, 63, v0
	s_lshl_b32 s3, s2, 12
	s_lshl_b32 s19, s2, 7
	v_lshlrev_b32_e32 v1, 11, v41
	v_lshl_or_b32 v1, v40, 2, v1
	v_lshlrev_b32_e32 v46, 4, v43
	v_lshl_add_u32 v35, v44, 16, v46
	v_lshl_add_u32 v35, v42, 21, v35
	v_add_u32_e32 v35, s19, v35
	v_lshlrev_b32_e32 v36, 2, v40
	v_lshl_add_u32 v36, v41, 18, v36
	v_lshl_add_u32 v36, v42, 21, v36
	v_add_u32_e32 v36, s19, v36
	v_mul_u32_u24_e32 v37, 0x1200, v42
	v_mul_u32_u24_e32 v38, 0x90, v44
	v_add3_u32 v38, v37, v38, v46
	v_mul_u32_u24_e32 v39, 0x90, v40
	v_lshlrev_b32_e32 v47, 6, v41
	v_add3_u32 v39, v37, v39, v47
	v_lshrrev_b32_e32 v46, 1, v44
	v_xor_b32_e32 v46, v43, v46
	v_lshlrev_b32_e32 v46, 4, v46
	v_lshl_add_u32 v35, v44, 16, v46
	v_lshl_add_u32 v35, v42, 21, v35
	v_add_u32_e32 v35, s19, v35
	v_xor_b32_e32 v86, 64, v35
	v_readfirstlane_b32 s23, v42
	v_bfe_u32 v47, v40, 1, 3
	v_lshlrev_b32_e32 v39, 2, v41
	v_xor_b32_e32 v39, v39, v47
	s_lshl_b32 s23, s23, 12
	v_lshlrev_b32_e32 v39, 4, v39
	v_lshl_add_u32 v39, v40, 7, v39
	v_lshl_add_u32 v39, v42, 12, v39
	s_mov_b32 m0, s23
	v_xor_b32_e32 v81, 16, v39
	v_xor_b32_e32 v82, 32, v39
	v_xor_b32_e32 v83, 48, v39
	v_cmp_gt_u32_e32 vcc, 32, v45
	v_mov_b32_e32 v34, 0xc1600000
	s_mov_b32 s16, 0x3fb8aa3b
	s_mov_b32 s17, 0x3f317218
	s_mov_b32 s20, 0x7fc00
	s_mov_b32 s21, 0xff800
	s_mov_b32 s22, 0x17f400
	s_lshl_b32 s24, 1, 16
	s_lshl_b32 s25, 2, 16
	s_lshl_b32 s26, 3, 16
	s_lshl_b32 s27, 8, 16
	s_lshl_b32 s28, 9, 16
	s_lshl_b32 s29, 10, 16
	s_lshl_b32 s30, 11, 16
	s_lshl_b32 s31, 16, 16
	s_lshl_b32 s32, 17, 16
	s_lshl_b32 s33, 18, 16
	s_lshl_b32 s34, 19, 16
	s_lshl_b32 s35, 24, 16
	s_lshl_b32 s36, 25, 16
	s_lshl_b32 s37, 26, 16
	s_lshl_b32 s38, 27, 16
	s_mov_b32 s14, 0x200000
	s_mov_b32 s15, 0x20000
	s_waitcnt lgkmcnt(0)
	s_mov_b32 s12, s6
	s_and_b32 s13, s7, 0xffff
	s_and_b32 s5, s5, 0xffff
	s_mov_b32 s6, 0x800000
	s_mov_b32 s7, s15
	s_and_b32 s9, s9, 0xffff
	s_mov_b32 s10, s6
	s_mov_b32 s11, s15
	buffer_load_dword v18, v1, s[12:15], s3 offen nt
	buffer_load_dword v19, v1, s[12:15], s3 offen offset:128 nt
	buffer_load_dword v20, v1, s[12:15], s3 offen offset:256 nt
	buffer_load_dword v21, v1, s[12:15], s3 offen offset:384 nt
	buffer_load_dword v22, v1, s[12:15], s3 offen offset:512 nt
	buffer_load_dword v23, v1, s[12:15], s3 offen offset:640 nt
	buffer_load_dword v24, v1, s[12:15], s3 offen offset:768 nt
	buffer_load_dword v25, v1, s[12:15], s3 offen offset:896 nt
	buffer_load_dword v26, v1, s[12:15], s3 offen offset:1024 nt
	buffer_load_dword v27, v1, s[12:15], s3 offen offset:1152 nt
	buffer_load_dword v28, v1, s[12:15], s3 offen offset:1280 nt
	buffer_load_dword v29, v1, s[12:15], s3 offen offset:1408 nt
	buffer_load_dword v30, v1, s[12:15], s3 offen offset:1536 nt
	buffer_load_dword v31, v1, s[12:15], s3 offen offset:1664 nt
	buffer_load_dword v32, v1, s[12:15], s3 offen offset:1792 nt
	buffer_load_dword v33, v1, s[12:15], s3 offen offset:1920 nt
	buffer_load_dwordx4 v35, s[4:7], 0 offen nt lds
	buffer_load_dwordx4 v86, s[4:7], s20 offen offset:1024 nt lds
	buffer_load_dwordx4 v35, s[4:7], s21 offen offset:2048 nt lds
	buffer_load_dwordx4 v86, s[4:7], s22 offen offset:3072 nt lds
	s_waitcnt vmcnt(4)
	v_max3_f32 v49, v18, v19, v20
	v_max3_f32 v50, v21, v22, v23
	v_max3_f32 v49, v49, v24, v25
	v_max3_f32 v50, v50, v26, v27
	v_max3_f32 v49, v49, v28, v29
	v_max3_f32 v50, v50, v30, v31
	v_max3_f32 v49, v49, v32, v33
	v_max_f32_e32 v49, v49, v50
	v_mov_b32_e32 v50, v49
	s_nop 1
	v_permlane32_swap_b32_e32 v49, v50
	v_max_f32_e32 v49, v49, v50
	v_fmamk_f32 v49, v49, 0x3fb8aa3b, v34
	v_fma_f32 v18, v18, s16, -v49
	v_exp_f32_e32 v18, v18
	v_fma_f32 v19, v19, s16, -v49
	v_exp_f32_e32 v19, v19
	v_fma_f32 v20, v20, s16, -v49
	v_exp_f32_e32 v20, v20
	v_fma_f32 v21, v21, s16, -v49
	v_exp_f32_e32 v21, v21
	v_fma_f32 v22, v22, s16, -v49
	v_exp_f32_e32 v22, v22
	v_fma_f32 v23, v23, s16, -v49
	v_exp_f32_e32 v23, v23
	v_fma_f32 v24, v24, s16, -v49
	v_exp_f32_e32 v24, v24
	v_fma_f32 v25, v25, s16, -v49
	v_exp_f32_e32 v25, v25
	v_fma_f32 v26, v26, s16, -v49
	v_exp_f32_e32 v26, v26
	v_fma_f32 v27, v27, s16, -v49
	v_exp_f32_e32 v27, v27
	v_fma_f32 v28, v28, s16, -v49
	v_exp_f32_e32 v28, v28
	v_fma_f32 v29, v29, s16, -v49
	v_exp_f32_e32 v29, v29
	v_fma_f32 v30, v30, s16, -v49
	v_exp_f32_e32 v30, v30
	v_fma_f32 v31, v31, s16, -v49
	v_exp_f32_e32 v31, v31
	v_fma_f32 v32, v32, s16, -v49
	v_exp_f32_e32 v32, v32
	v_fma_f32 v33, v33, s16, -v49
	v_exp_f32_e32 v33, v33
	v_add_f32_e32 v50, v18, v19
	v_add_f32_e32 v51, v20, v21
	v_add_f32_e32 v50, v50, v22
	v_add_f32_e32 v51, v51, v23
	v_add_f32_e32 v50, v50, v24
	v_add_f32_e32 v51, v51, v25
	v_add_f32_e32 v50, v50, v26
	v_add_f32_e32 v51, v51, v27
	v_add_f32_e32 v50, v50, v28
	v_add_f32_e32 v51, v51, v29
	v_add_f32_e32 v50, v50, v30
	v_add_f32_e32 v51, v51, v31
	v_add_f32_e32 v50, v50, v32
	v_add_f32_e32 v51, v51, v33
	v_add_f32_e32 v50, v50, v51
	v_mov_b32_e32 v51, v50
	s_nop 1
	v_permlane32_swap_b32_e32 v50, v51
	v_add_f32_e32 v50, v50, v51
	v_log_f32_e32 v50, v50
	v_cvt_pk_f16_f32 v40, v18, v19
	v_cvt_pk_f16_f32 v41, v20, v21
	v_cvt_pk_f16_f32 v42, v22, v23
	v_cvt_pk_f16_f32 v43, v24, v25
	v_cvt_pk_f16_f32 v44, v26, v27
	v_cvt_pk_f16_f32 v45, v28, v29
	v_cvt_pk_f16_f32 v46, v30, v31
	v_cvt_pk_f16_f32 v47, v32, v33
	v_add_f32_e32 v50, 0x41600000, v50
	v_mul_f32_e32 v50, 0xbf317218, v50
	v_cndmask_b32_e64 v51, v50, 1.0, vcc
	s_waitcnt vmcnt(0)
	ds_read_b128 v[2:5], v39
	ds_read_b128 v[6:9], v81
	ds_read_b128 v[10:13], v82
	ds_read_b128 v[14:17], v83
	s_waitcnt lgkmcnt(2)
	v_max3_f32 v52, v2, v3, v4
	v_max3_f32 v53, v5, v6, v7
	v_max_f32_e32 v52, v52, v8
	v_max_f32_e32 v53, v53, v9
	s_waitcnt lgkmcnt(0)
	v_max3_f32 v52, v52, v10, v11
	v_max3_f32 v53, v53, v12, v13
	v_max3_f32 v52, v52, v14, v15
	v_max3_f32 v53, v53, v16, v17
	v_max_f32_e32 v52, v52, v53
	v_mov_b32_e32 v53, v52
	s_nop 1
	v_permlane32_swap_b32_e32 v52, v53
	v_max_f32_e32 v52, v52, v53
	v_cndmask_b32_e32 v54, 1.0, v52, vcc
	v_fmamk_f32 v55, v52, 0x3fb8aa3b, v34
	v_fma_f32 v2, v2, s16, -v55
	v_mfma_f32_32x32x2_f32 v[64:79], v54, v51, 0
	v_exp_f32_e32 v2, v2
	v_fma_f32 v3, v3, s16, -v55
	v_exp_f32_e32 v3, v3
	v_fma_f32 v4, v4, s16, -v55
	v_exp_f32_e32 v4, v4
	v_fma_f32 v5, v5, s16, -v55
	v_exp_f32_e32 v5, v5
	v_fma_f32 v6, v6, s16, -v55
	v_exp_f32_e32 v6, v6
	v_fma_f32 v7, v7, s16, -v55
	v_exp_f32_e32 v7, v7
	v_fma_f32 v8, v8, s16, -v55
	v_exp_f32_e32 v8, v8
	v_fma_f32 v9, v9, s16, -v55
	v_exp_f32_e32 v9, v9
	v_fma_f32 v10, v10, s16, -v55
	v_exp_f32_e32 v10, v10
	v_cvt_pk_f16_f32 v56, v2, v3
	v_cvt_pk_f16_f32 v57, v4, v5
	v_cvt_pk_f16_f32 v58, v6, v7
	v_cvt_pk_f16_f32 v59, v8, v9
	v_fma_f32 v11, v11, s16, -v55
	v_exp_f32_e32 v11, v11
	v_fma_f32 v12, v12, s16, -v55
	v_exp_f32_e32 v12, v12
	v_mfma_f32_32x32x16_f16 v[18:33], v[56:59], v[40:43], 0
	v_fma_f32 v13, v13, s16, -v55
	v_exp_f32_e32 v13, v13
	v_fma_f32 v14, v14, s16, -v55
	v_exp_f32_e32 v14, v14
	v_fma_f32 v15, v15, s16, -v55
	v_exp_f32_e32 v15, v15
	v_fma_f32 v16, v16, s16, -v55
	v_exp_f32_e32 v16, v16
	v_fma_f32 v17, v17, s16, -v55
	v_exp_f32_e32 v17, v17
	v_cvt_pk_f16_f32 v60, v10, v11
	v_cvt_pk_f16_f32 v61, v12, v13
	v_cvt_pk_f16_f32 v62, v14, v15
	v_cvt_pk_f16_f32 v63, v16, v17
	s_nop 1
	v_mfma_f32_32x32x16_f16 v[18:33], v[60:63], v[44:47], v[18:33]
	s_nop 11
	v_log_f32_e32 v18, v18
	v_log_f32_e32 v19, v19
	v_log_f32_e32 v20, v20
	v_fmac_f32_e32 v64, s17, v18
	buffer_store_dword v64, v36, s[8:11], 0 offen nt
	v_log_f32_e32 v21, v21
	v_fmac_f32_e32 v65, s17, v19
	buffer_store_dword v65, v36, s[8:11], s24 offen nt
	v_log_f32_e32 v22, v22
	v_fmac_f32_e32 v66, s17, v20
	buffer_store_dword v66, v36, s[8:11], s25 offen nt
	v_log_f32_e32 v23, v23
	v_fmac_f32_e32 v67, s17, v21
	buffer_store_dword v67, v36, s[8:11], s26 offen nt
	v_log_f32_e32 v24, v24
	v_fmac_f32_e32 v68, s17, v22
	buffer_store_dword v68, v36, s[8:11], s27 offen nt
	v_log_f32_e32 v25, v25
	v_fmac_f32_e32 v69, s17, v23
	buffer_store_dword v69, v36, s[8:11], s28 offen nt
	v_log_f32_e32 v26, v26
	v_fmac_f32_e32 v70, s17, v24
	buffer_store_dword v70, v36, s[8:11], s29 offen nt
	v_log_f32_e32 v27, v27
	v_fmac_f32_e32 v71, s17, v25
	buffer_store_dword v71, v36, s[8:11], s30 offen nt
	v_log_f32_e32 v28, v28
	v_fmac_f32_e32 v72, s17, v26
	buffer_store_dword v72, v36, s[8:11], s31 offen nt
	v_log_f32_e32 v29, v29
	v_fmac_f32_e32 v73, s17, v27
	buffer_store_dword v73, v36, s[8:11], s32 offen nt
	v_log_f32_e32 v30, v30
	v_fmac_f32_e32 v74, s17, v28
	buffer_store_dword v74, v36, s[8:11], s33 offen nt
	v_log_f32_e32 v31, v31
	v_fmac_f32_e32 v75, s17, v29
	buffer_store_dword v75, v36, s[8:11], s34 offen nt
	v_log_f32_e32 v32, v32
	v_fmac_f32_e32 v76, s17, v30
	buffer_store_dword v76, v36, s[8:11], s35 offen nt
	v_log_f32_e32 v33, v33
	v_fmac_f32_e32 v77, s17, v31
	buffer_store_dword v77, v36, s[8:11], s36 offen nt
	v_fmac_f32_e32 v78, s17, v32
	buffer_store_dword v78, v36, s[8:11], s37 offen nt
	v_fmac_f32_e32 v79, s17, v33
	buffer_store_dword v79, v36, s[8:11], s38 offen nt
	s_endpgm
